# light-tile K-loops: fragment reads of the MFMA section software-pipelined two steps ahead (3-slot A-fragment ring), straight-line mlim exits
# speedup vs baseline: 1.0046x; 1.0046x over previous
; #define LAS __attribute__((address_space(3)))
; __device__ __forceinline__ void gemm_kloop_light(f32x4 (&acc)[8][4], LAS unsigned char* lds, const GemmT& T, ...
;     ...
;         if (mlim > 0) {
; #pragma unroll
;             for (int ks = 0; ks < 2; ++ks) { const LAS unsigned char* s_ = lds + cur * 65536 + ks * 1024; bf16x8 Bf_[4];
; #pragma unroll
;                 for (int n_ = 0; n_ < 4; ++n_) Bf_[n_] = *(const LAS bf16x8*)(s_ + T.b_r + n_ * 2048);
; #pragma unroll
;                 for (int m_ = 0; m_ < 8; ++m_) if (m_ < mlim) { const bf16x8 At_ = *(const LAS bf16x8*)(s_ + T.a_r + m_ * 2048);
; #pragma unroll
;                     for (int n_ = 0; n_ < 4; ++n_) acc[m_][n_] = __builtin_amdgcn_mfma_f32_16x16x32_bf16(Bf_[n_], At_, acc[m_][n_], 0, 0, 0); } } }
.LBB0_1175:
	s_and_b32 s6, s68, 0x10000
	s_xor_b32 s71, s6, 0x10000
	v_cndmask_b32_e64 v3, 0, 1, s[62:63]
	s_andn2_b64 vcc, exec, s[62:63]
	v_cmp_ne_u32_e64 s[4:5], 1, v3
	s_cbranch_vccnz .LBB0_1174
	s_add_i32 s6, s6, 0
	v_add_u32_e32 v4, s6, v226
	v_add_u32_e32 v3, s6, v216
	ds_read_b128 v[198:201], v4 offset:32768
	ds_read_b128 v[202:205], v4 offset:34816
	ds_read_b128 v[206:209], v4 offset:36864
	ds_read_b128 v[210:213], v4 offset:38912
	ds_read_b128 v[230:233], v3
	ds_read_b128 v[248:251], v3 offset:2048
	ds_read_b128 v[252:255], v3 offset:4096
	s_waitcnt lgkmcnt(2)
	v_mfma_f32_16x16x32_bf16 v[154:157], v[198:201], v[230:233], v[154:157]
	v_mfma_f32_16x16x32_bf16 v[194:197], v[202:205], v[230:233], v[194:197]
	v_mfma_f32_16x16x32_bf16 v[150:153], v[206:209], v[230:233], v[150:153]
	v_mfma_f32_16x16x32_bf16 v[158:161], v[210:213], v[230:233], v[158:161]
	s_cmp_eq_u32 s1, 1
	s_cbranch_scc1 .Lmy_mmg_k0
	ds_read_b128 v[230:233], v3 offset:6144
	s_waitcnt lgkmcnt(2)
	v_mfma_f32_16x16x32_bf16 v[106:109], v[198:201], v[248:251], v[106:109]
	v_mfma_f32_16x16x32_bf16 v[138:141], v[202:205], v[248:251], v[138:141]
	v_mfma_f32_16x16x32_bf16 v[102:105], v[206:209], v[248:251], v[102:105]
	v_mfma_f32_16x16x32_bf16 v[110:113], v[210:213], v[248:251], v[110:113]
	s_cmp_eq_u32 s1, 2
	s_cbranch_scc1 .Lmy_mmg_k0
	ds_read_b128 v[248:251], v3 offset:8192
	s_waitcnt lgkmcnt(2)
	v_mfma_f32_16x16x32_bf16 v[90:93], v[198:201], v[252:255], v[90:93]
	v_mfma_f32_16x16x32_bf16 v[98:101], v[202:205], v[252:255], v[98:101]
	v_mfma_f32_16x16x32_bf16 v[86:89], v[206:209], v[252:255], v[86:89]
	v_mfma_f32_16x16x32_bf16 v[94:97], v[210:213], v[252:255], v[94:97]
	s_cmp_eq_u32 s1, 3
	s_cbranch_scc1 .Lmy_mmg_k0
	ds_read_b128 v[252:255], v3 offset:10240
	s_waitcnt lgkmcnt(2)
	v_mfma_f32_16x16x32_bf16 v[74:77], v[198:201], v[230:233], v[74:77]
	v_mfma_f32_16x16x32_bf16 v[82:85], v[202:205], v[230:233], v[82:85]
	v_mfma_f32_16x16x32_bf16 v[70:73], v[206:209], v[230:233], v[70:73]
	v_mfma_f32_16x16x32_bf16 v[78:81], v[210:213], v[230:233], v[78:81]
	s_cmp_eq_u32 s1, 4
	s_cbranch_scc1 .Lmy_mmg_k0
	ds_read_b128 v[230:233], v3 offset:12288
	s_waitcnt lgkmcnt(2)
	v_mfma_f32_16x16x32_bf16 v[58:61], v[198:201], v[248:251], v[58:61]
	v_mfma_f32_16x16x32_bf16 v[66:69], v[202:205], v[248:251], v[66:69]
	v_mfma_f32_16x16x32_bf16 v[54:57], v[206:209], v[248:251], v[54:57]
	v_mfma_f32_16x16x32_bf16 v[62:65], v[210:213], v[248:251], v[62:65]
	s_cmp_eq_u32 s1, 5
	s_cbranch_scc1 .Lmy_mmg_k0
	ds_read_b128 v[248:251], v3 offset:14336
	s_waitcnt lgkmcnt(2)
	v_mfma_f32_16x16x32_bf16 v[42:45], v[198:201], v[252:255], v[42:45]
	v_mfma_f32_16x16x32_bf16 v[50:53], v[202:205], v[252:255], v[50:53]
	v_mfma_f32_16x16x32_bf16 v[38:41], v[206:209], v[252:255], v[38:41]
	v_mfma_f32_16x16x32_bf16 v[46:49], v[210:213], v[252:255], v[46:49]
	s_cmp_eq_u32 s1, 6
	s_cbranch_scc1 .Lmy_mmg_k0
	s_waitcnt lgkmcnt(1)
	v_mfma_f32_16x16x32_bf16 v[26:29], v[198:201], v[230:233], v[26:29]
	v_mfma_f32_16x16x32_bf16 v[34:37], v[202:205], v[230:233], v[34:37]
	v_mfma_f32_16x16x32_bf16 v[22:25], v[206:209], v[230:233], v[22:25]
	v_mfma_f32_16x16x32_bf16 v[30:33], v[210:213], v[230:233], v[30:33]
	s_cmp_eq_u32 s1, 7
	s_cbranch_scc1 .Lmy_mmg_k0
	s_waitcnt lgkmcnt(0)
	v_mfma_f32_16x16x32_bf16 v[10:13], v[198:201], v[248:251], v[10:13]
	v_mfma_f32_16x16x32_bf16 v[18:21], v[202:205], v[248:251], v[18:21]
	v_mfma_f32_16x16x32_bf16 v[6:9], v[206:209], v[248:251], v[6:9]
	v_mfma_f32_16x16x32_bf16 v[14:17], v[210:213], v[248:251], v[14:17]
; #define LAS __attribute__((address_space(3)))
; __device__ __forceinline__ void gemm_kloop_light(f32x4 (&acc)[8][4], LAS unsigned char* lds, const GemmT& T, ...
;     ...
;         if (mlim > 0) {
; #pragma unroll
;             for (int ks = 0; ks < 2; ++ks) { const LAS unsigned char* s_ = lds + cur * 65536 + ks * 1024; bf16x8 Bf_[4];
; #pragma unroll
;                 for (int n_ = 0; n_ < 4; ++n_) Bf_[n_] = *(const LAS bf16x8*)(s_ + T.b_r + n_ * 2048);
; #pragma unroll
;                 for (int m_ = 0; m_ < 8; ++m_) if (m_ < mlim) { const bf16x8 At_ = *(const LAS bf16x8*)(s_ + T.a_r + m_ * 2048);
; #pragma unroll
;                     for (int n_ = 0; n_ < 4; ++n_) acc[m_][n_] = __builtin_amdgcn_mfma_f32_16x16x32_bf16(Bf_[n_], At_, acc[m_][n_], 0, 0, 0); } } }
.Lmy_mmg_k0:
	ds_read_b128 v[198:201], v4 offset:33792
	ds_read_b128 v[202:205], v4 offset:35840
	ds_read_b128 v[206:209], v4 offset:37888
	ds_read_b128 v[210:213], v4 offset:39936
	ds_read_b128 v[230:233], v3 offset:1024
	ds_read_b128 v[248:251], v3 offset:3072
	ds_read_b128 v[252:255], v3 offset:5120
	s_waitcnt lgkmcnt(2)
	v_mfma_f32_16x16x32_bf16 v[154:157], v[198:201], v[230:233], v[154:157]
	v_mfma_f32_16x16x32_bf16 v[194:197], v[202:205], v[230:233], v[194:197]
	v_mfma_f32_16x16x32_bf16 v[150:153], v[206:209], v[230:233], v[150:153]
	v_mfma_f32_16x16x32_bf16 v[158:161], v[210:213], v[230:233], v[158:161]
	s_cmp_eq_u32 s1, 1
	s_cbranch_scc1 .Lmy_mmg_k1
	ds_read_b128 v[230:233], v3 offset:7168
	s_waitcnt lgkmcnt(2)
	v_mfma_f32_16x16x32_bf16 v[106:109], v[198:201], v[248:251], v[106:109]
	v_mfma_f32_16x16x32_bf16 v[138:141], v[202:205], v[248:251], v[138:141]
	v_mfma_f32_16x16x32_bf16 v[102:105], v[206:209], v[248:251], v[102:105]
	v_mfma_f32_16x16x32_bf16 v[110:113], v[210:213], v[248:251], v[110:113]
	s_cmp_eq_u32 s1, 2
	s_cbranch_scc1 .Lmy_mmg_k1
	ds_read_b128 v[248:251], v3 offset:9216
	s_waitcnt lgkmcnt(2)
	v_mfma_f32_16x16x32_bf16 v[90:93], v[198:201], v[252:255], v[90:93]
	v_mfma_f32_16x16x32_bf16 v[98:101], v[202:205], v[252:255], v[98:101]
	v_mfma_f32_16x16x32_bf16 v[86:89], v[206:209], v[252:255], v[86:89]
	v_mfma_f32_16x16x32_bf16 v[94:97], v[210:213], v[252:255], v[94:97]
	s_cmp_eq_u32 s1, 3
	s_cbranch_scc1 .Lmy_mmg_k1
	ds_read_b128 v[252:255], v3 offset:11264
	s_waitcnt lgkmcnt(2)
	v_mfma_f32_16x16x32_bf16 v[74:77], v[198:201], v[230:233], v[74:77]
	v_mfma_f32_16x16x32_bf16 v[82:85], v[202:205], v[230:233], v[82:85]
	v_mfma_f32_16x16x32_bf16 v[70:73], v[206:209], v[230:233], v[70:73]
	v_mfma_f32_16x16x32_bf16 v[78:81], v[210:213], v[230:233], v[78:81]
	s_cmp_eq_u32 s1, 4
	s_cbranch_scc1 .Lmy_mmg_k1
	ds_read_b128 v[230:233], v3 offset:13312
	s_waitcnt lgkmcnt(2)
	v_mfma_f32_16x16x32_bf16 v[58:61], v[198:201], v[248:251], v[58:61]
	v_mfma_f32_16x16x32_bf16 v[66:69], v[202:205], v[248:251], v[66:69]
	v_mfma_f32_16x16x32_bf16 v[54:57], v[206:209], v[248:251], v[54:57]
	v_mfma_f32_16x16x32_bf16 v[62:65], v[210:213], v[248:251], v[62:65]
	s_cmp_eq_u32 s1, 5
	s_cbranch_scc1 .Lmy_mmg_k1
	ds_read_b128 v[248:251], v3 offset:15360
	s_waitcnt lgkmcnt(2)
	v_mfma_f32_16x16x32_bf16 v[42:45], v[198:201], v[252:255], v[42:45]
	v_mfma_f32_16x16x32_bf16 v[50:53], v[202:205], v[252:255], v[50:53]
	v_mfma_f32_16x16x32_bf16 v[38:41], v[206:209], v[252:255], v[38:41]
	v_mfma_f32_16x16x32_bf16 v[46:49], v[210:213], v[252:255], v[46:49]
	s_cmp_eq_u32 s1, 6
	s_cbranch_scc1 .Lmy_mmg_k1
	s_waitcnt lgkmcnt(1)
	v_mfma_f32_16x16x32_bf16 v[26:29], v[198:201], v[230:233], v[26:29]
	v_mfma_f32_16x16x32_bf16 v[34:37], v[202:205], v[230:233], v[34:37]
	v_mfma_f32_16x16x32_bf16 v[22:25], v[206:209], v[230:233], v[22:25]
	v_mfma_f32_16x16x32_bf16 v[30:33], v[210:213], v[230:233], v[30:33]
	s_cmp_eq_u32 s1, 7
	s_cbranch_scc1 .Lmy_mmg_k1
	s_waitcnt lgkmcnt(0)
	v_mfma_f32_16x16x32_bf16 v[10:13], v[198:201], v[248:251], v[10:13]
	v_mfma_f32_16x16x32_bf16 v[18:21], v[202:205], v[248:251], v[18:21]
	v_mfma_f32_16x16x32_bf16 v[6:9], v[206:209], v[248:251], v[6:9]
	v_mfma_f32_16x16x32_bf16 v[14:17], v[210:213], v[248:251], v[14:17]
.Lmy_mmg_k1:
	s_branch .LBB0_1174
.LBB0_1204:
	s_add_i32 s6, s3, 0x16000
	s_add_i32 s7, s3, 0x14000
	s_add_i32 s3, s3, 0x12000
	s_mov_b32 s38, s26
	s_mov_b32 s39, s27
	v_cndmask_b32_e64 v3, 0, 1, s[60:61]
	s_and_b64 vcc, exec, s[4:5]
	v_cmp_ne_u32_e64 s[6:7], 1, v3
	s_cbranch_vccnz .LBB0_1221
	v_add_u32_e32 v4, 0, v226
	ds_read_b128 v[198:201], v4 offset:32768
	v_add_u32_e32 v3, 0, v216
	ds_read_b128 v[202:205], v4 offset:34816
	ds_read_b128 v[230:233], v3
	ds_read_b128 v[206:209], v4 offset:36864
	ds_read_b128 v[210:213], v4 offset:38912
	s_waitcnt lgkmcnt(2)
	v_mfma_f32_16x16x32_bf16 v[194:197], v[202:205], v[230:233], v[194:197]
	s_and_b64 vcc, exec, s[6:7]
	v_mfma_f32_16x16x32_bf16 v[154:157], v[198:201], v[230:233], v[154:157]
	s_waitcnt lgkmcnt(1)
	v_mfma_f32_16x16x32_bf16 v[150:153], v[206:209], v[230:233], v[150:153]
	s_waitcnt lgkmcnt(0)
	v_mfma_f32_16x16x32_bf16 v[158:161], v[210:213], v[230:233], v[158:161]
	s_cbranch_vccnz .LBB0_1239
	ds_read_b128 v[230:233], v3 offset:2048
	s_waitcnt lgkmcnt(0)
	v_mfma_f32_16x16x32_bf16 v[106:109], v[198:201], v[230:233], v[106:109]
	v_mfma_f32_16x16x32_bf16 v[138:141], v[202:205], v[230:233], v[138:141]
	v_mfma_f32_16x16x32_bf16 v[102:105], v[206:209], v[230:233], v[102:105]
	v_mfma_f32_16x16x32_bf16 v[110:113], v[210:213], v[230:233], v[110:113]
	v_cndmask_b32_e64 v5, 0, 1, s[58:59]
	v_cmp_ne_u32_e64 s[8:9], 1, v5
	s_andn2_b64 vcc, exec, s[58:59]
	s_cbranch_vccz .LBB0_1240

; #define LAS __attribute__((address_space(3)))
; __device__ __forceinline__ void gemm_kloop_light(f32x4 (&acc)[8][4], LAS unsigned char* lds, const GemmT& T, ...
;     ...
;             for (int ks = 0; ks < 2; ++ks) { const LAS unsigned char* s_ = lds + cur * 65536 + ks * 1024; bf16x8 Bf_[4];
; #pragma unroll
;                 for (int n_ = 0; n_ < 4; ++n_) Bf_[n_] = *(const LAS bf16x8*)(s_ + T.b_r + n_ * 2048);
; #pragma unroll
;                 for (int m_ = 0; m_ < 8; ++m_) if (m_ < mlim) { const bf16x8 At_ = *(const LAS bf16x8*)(s_ + T.a_r + m_ * 2048);
; #pragma unroll
;                     for (int n_ = 0; n_ < 4; ++n_) acc[m_][n_] = __builtin_amdgcn_mfma_f32_16x16x32_bf16(Bf_[n_], At_, acc[m_][n_], 0, 0, 0); } } }
.LBB0_1486:
	s_and_b32 s6, s3, 0x10000
	s_xor_b32 s74, s6, 0x10000
	v_cndmask_b32_e64 v3, 0, 1, s[60:61]
	s_andn2_b64 vcc, exec, s[60:61]
	v_cmp_ne_u32_e64 s[4:5], 1, v3
	s_cbranch_vccnz .LBB0_1485
	s_add_i32 s6, s6, 0
	v_add_u32_e32 v4, s6, v227
	v_add_u32_e32 v3, s6, v217
	ds_read_b128 v[198:201], v4 offset:32768
	ds_read_b128 v[202:205], v4 offset:34816
	ds_read_b128 v[206:209], v4 offset:36864
	ds_read_b128 v[210:213], v4 offset:38912
	ds_read_b128 v[232:235], v3
	ds_read_b128 v[248:251], v3 offset:2048
	ds_read_b128 v[252:255], v3 offset:4096
	s_waitcnt lgkmcnt(2)
	v_mfma_f32_16x16x32_bf16 v[158:161], v[198:201], v[232:235], v[158:161]
	v_mfma_f32_16x16x32_bf16 v[166:169], v[202:205], v[232:235], v[166:169]
	v_mfma_f32_16x16x32_bf16 v[150:153], v[206:209], v[232:235], v[150:153]
	v_mfma_f32_16x16x32_bf16 v[154:157], v[210:213], v[232:235], v[154:157]
	s_cmp_eq_u32 s1, 1
	s_cbranch_scc1 .Lmy_mmd_k0
	ds_read_b128 v[232:235], v3 offset:6144
	s_waitcnt lgkmcnt(2)
	v_mfma_f32_16x16x32_bf16 v[134:137], v[198:201], v[248:251], v[134:137]
	v_mfma_f32_16x16x32_bf16 v[146:149], v[202:205], v[248:251], v[146:149]
	v_mfma_f32_16x16x32_bf16 v[102:105], v[206:209], v[248:251], v[102:105]
	v_mfma_f32_16x16x32_bf16 v[106:109], v[210:213], v[248:251], v[106:109]
	s_cmp_eq_u32 s1, 2
	s_cbranch_scc1 .Lmy_mmd_k0
	ds_read_b128 v[248:251], v3 offset:8192
	s_waitcnt lgkmcnt(2)
	v_mfma_f32_16x16x32_bf16 v[94:97], v[198:201], v[252:255], v[94:97]
	v_mfma_f32_16x16x32_bf16 v[98:101], v[202:205], v[252:255], v[98:101]
	v_mfma_f32_16x16x32_bf16 v[86:89], v[206:209], v[252:255], v[86:89]
	v_mfma_f32_16x16x32_bf16 v[90:93], v[210:213], v[252:255], v[90:93]
	s_cmp_eq_u32 s1, 3
	s_cbranch_scc1 .Lmy_mmd_k0
	ds_read_b128 v[252:255], v3 offset:10240
	s_waitcnt lgkmcnt(2)
	v_mfma_f32_16x16x32_bf16 v[78:81], v[198:201], v[232:235], v[78:81]
	v_mfma_f32_16x16x32_bf16 v[82:85], v[202:205], v[232:235], v[82:85]
	v_mfma_f32_16x16x32_bf16 v[70:73], v[206:209], v[232:235], v[70:73]
	v_mfma_f32_16x16x32_bf16 v[74:77], v[210:213], v[232:235], v[74:77]
	s_cmp_eq_u32 s1, 4
	s_cbranch_scc1 .Lmy_mmd_k0
	ds_read_b128 v[232:235], v3 offset:12288
	s_waitcnt lgkmcnt(2)
	v_mfma_f32_16x16x32_bf16 v[62:65], v[198:201], v[248:251], v[62:65]
	v_mfma_f32_16x16x32_bf16 v[66:69], v[202:205], v[248:251], v[66:69]
	v_mfma_f32_16x16x32_bf16 v[54:57], v[206:209], v[248:251], v[54:57]
	v_mfma_f32_16x16x32_bf16 v[58:61], v[210:213], v[248:251], v[58:61]
	s_cmp_eq_u32 s1, 5
	s_cbranch_scc1 .Lmy_mmd_k0
	ds_read_b128 v[248:251], v3 offset:14336
	s_waitcnt lgkmcnt(2)
	v_mfma_f32_16x16x32_bf16 v[46:49], v[198:201], v[252:255], v[46:49]
	v_mfma_f32_16x16x32_bf16 v[50:53], v[202:205], v[252:255], v[50:53]
	v_mfma_f32_16x16x32_bf16 v[38:41], v[206:209], v[252:255], v[38:41]
	v_mfma_f32_16x16x32_bf16 v[42:45], v[210:213], v[252:255], v[42:45]
	s_cmp_eq_u32 s1, 6
	s_cbranch_scc1 .Lmy_mmd_k0
	s_waitcnt lgkmcnt(1)
	v_mfma_f32_16x16x32_bf16 v[30:33], v[198:201], v[232:235], v[30:33]
	v_mfma_f32_16x16x32_bf16 v[34:37], v[202:205], v[232:235], v[34:37]
	v_mfma_f32_16x16x32_bf16 v[22:25], v[206:209], v[232:235], v[22:25]
	v_mfma_f32_16x16x32_bf16 v[26:29], v[210:213], v[232:235], v[26:29]
	s_cmp_eq_u32 s1, 7
	s_cbranch_scc1 .Lmy_mmd_k0
	s_waitcnt lgkmcnt(0)
	v_mfma_f32_16x16x32_bf16 v[14:17], v[198:201], v[248:251], v[14:17]
	v_mfma_f32_16x16x32_bf16 v[18:21], v[202:205], v[248:251], v[18:21]
	v_mfma_f32_16x16x32_bf16 v[6:9], v[206:209], v[248:251], v[6:9]
	v_mfma_f32_16x16x32_bf16 v[10:13], v[210:213], v[248:251], v[10:13]
; #define LAS __attribute__((address_space(3)))
; __device__ __forceinline__ void gemm_kloop_light(f32x4 (&acc)[8][4], LAS unsigned char* lds, const GemmT& T, ...
;     ...
;             for (int ks = 0; ks < 2; ++ks) { const LAS unsigned char* s_ = lds + cur * 65536 + ks * 1024; bf16x8 Bf_[4];
; #pragma unroll
;                 for (int n_ = 0; n_ < 4; ++n_) Bf_[n_] = *(const LAS bf16x8*)(s_ + T.b_r + n_ * 2048);
; #pragma unroll
;                 for (int m_ = 0; m_ < 8; ++m_) if (m_ < mlim) { const bf16x8 At_ = *(const LAS bf16x8*)(s_ + T.a_r + m_ * 2048);
; #pragma unroll
;                     for (int n_ = 0; n_ < 4; ++n_) acc[m_][n_] = __builtin_amdgcn_mfma_f32_16x16x32_bf16(Bf_[n_], At_, acc[m_][n_], 0, 0, 0); } } }
.Lmy_mmd_k0:
	ds_read_b128 v[198:201], v4 offset:33792
	ds_read_b128 v[202:205], v4 offset:35840
	ds_read_b128 v[206:209], v4 offset:37888
	ds_read_b128 v[210:213], v4 offset:39936
	ds_read_b128 v[232:235], v3 offset:1024
	ds_read_b128 v[248:251], v3 offset:3072
	ds_read_b128 v[252:255], v3 offset:5120
	s_waitcnt lgkmcnt(2)
	v_mfma_f32_16x16x32_bf16 v[158:161], v[198:201], v[232:235], v[158:161]
	v_mfma_f32_16x16x32_bf16 v[166:169], v[202:205], v[232:235], v[166:169]
	v_mfma_f32_16x16x32_bf16 v[150:153], v[206:209], v[232:235], v[150:153]
	v_mfma_f32_16x16x32_bf16 v[154:157], v[210:213], v[232:235], v[154:157]
	s_cmp_eq_u32 s1, 1
	s_cbranch_scc1 .Lmy_mmd_k1
	ds_read_b128 v[232:235], v3 offset:7168
	s_waitcnt lgkmcnt(2)
	v_mfma_f32_16x16x32_bf16 v[134:137], v[198:201], v[248:251], v[134:137]
	v_mfma_f32_16x16x32_bf16 v[146:149], v[202:205], v[248:251], v[146:149]
	v_mfma_f32_16x16x32_bf16 v[102:105], v[206:209], v[248:251], v[102:105]
	v_mfma_f32_16x16x32_bf16 v[106:109], v[210:213], v[248:251], v[106:109]
	s_cmp_eq_u32 s1, 2
	s_cbranch_scc1 .Lmy_mmd_k1
	ds_read_b128 v[248:251], v3 offset:9216
	s_waitcnt lgkmcnt(2)
	v_mfma_f32_16x16x32_bf16 v[94:97], v[198:201], v[252:255], v[94:97]
	v_mfma_f32_16x16x32_bf16 v[98:101], v[202:205], v[252:255], v[98:101]
	v_mfma_f32_16x16x32_bf16 v[86:89], v[206:209], v[252:255], v[86:89]
	v_mfma_f32_16x16x32_bf16 v[90:93], v[210:213], v[252:255], v[90:93]
	s_cmp_eq_u32 s1, 3
	s_cbranch_scc1 .Lmy_mmd_k1
	ds_read_b128 v[252:255], v3 offset:11264
	s_waitcnt lgkmcnt(2)
	v_mfma_f32_16x16x32_bf16 v[78:81], v[198:201], v[232:235], v[78:81]
	v_mfma_f32_16x16x32_bf16 v[82:85], v[202:205], v[232:235], v[82:85]
	v_mfma_f32_16x16x32_bf16 v[70:73], v[206:209], v[232:235], v[70:73]
	v_mfma_f32_16x16x32_bf16 v[74:77], v[210:213], v[232:235], v[74:77]
	s_cmp_eq_u32 s1, 4
	s_cbranch_scc1 .Lmy_mmd_k1
	ds_read_b128 v[232:235], v3 offset:13312
	s_waitcnt lgkmcnt(2)
	v_mfma_f32_16x16x32_bf16 v[62:65], v[198:201], v[248:251], v[62:65]
	v_mfma_f32_16x16x32_bf16 v[66:69], v[202:205], v[248:251], v[66:69]
	v_mfma_f32_16x16x32_bf16 v[54:57], v[206:209], v[248:251], v[54:57]
	v_mfma_f32_16x16x32_bf16 v[58:61], v[210:213], v[248:251], v[58:61]
	s_cmp_eq_u32 s1, 5
	s_cbranch_scc1 .Lmy_mmd_k1
	ds_read_b128 v[248:251], v3 offset:15360
	s_waitcnt lgkmcnt(2)
	v_mfma_f32_16x16x32_bf16 v[46:49], v[198:201], v[252:255], v[46:49]
	v_mfma_f32_16x16x32_bf16 v[50:53], v[202:205], v[252:255], v[50:53]
	v_mfma_f32_16x16x32_bf16 v[38:41], v[206:209], v[252:255], v[38:41]
	v_mfma_f32_16x16x32_bf16 v[42:45], v[210:213], v[252:255], v[42:45]
	s_cmp_eq_u32 s1, 6
	s_cbranch_scc1 .Lmy_mmd_k1
	s_waitcnt lgkmcnt(1)
	v_mfma_f32_16x16x32_bf16 v[30:33], v[198:201], v[232:235], v[30:33]
	v_mfma_f32_16x16x32_bf16 v[34:37], v[202:205], v[232:235], v[34:37]
	v_mfma_f32_16x16x32_bf16 v[22:25], v[206:209], v[232:235], v[22:25]
	v_mfma_f32_16x16x32_bf16 v[26:29], v[210:213], v[232:235], v[26:29]
	s_cmp_eq_u32 s1, 7
	s_cbranch_scc1 .Lmy_mmd_k1
	s_waitcnt lgkmcnt(0)
	v_mfma_f32_16x16x32_bf16 v[14:17], v[198:201], v[248:251], v[14:17]
	v_mfma_f32_16x16x32_bf16 v[18:21], v[202:205], v[248:251], v[18:21]
	v_mfma_f32_16x16x32_bf16 v[6:9], v[206:209], v[248:251], v[6:9]
	v_mfma_f32_16x16x32_bf16 v[10:13], v[210:213], v[248:251], v[10:13]
.Lmy_mmd_k1:
	s_branch .LBB0_1485
.LBB0_1515:
	s_add_i32 s3, s2, 0x16000
	s_add_i32 s6, s2, 0x14000
	s_add_i32 s2, s2, 0x12000
	s_mov_b32 s38, s26
	s_mov_b32 s39, s27
	v_cndmask_b32_e64 v3, 0, 1, s[58:59]
	s_and_b64 vcc, exec, s[4:5]
	v_cmp_ne_u32_e64 s[6:7], 1, v3
	s_cbranch_vccnz .LBB0_1532
	v_add_u32_e32 v4, 0, v227
	ds_read_b128 v[198:201], v4 offset:32768
	v_add_u32_e32 v3, 0, v217
	ds_read_b128 v[202:205], v4 offset:34816
	ds_read_b128 v[232:235], v3
	ds_read_b128 v[206:209], v4 offset:36864
	ds_read_b128 v[210:213], v4 offset:38912
	s_waitcnt lgkmcnt(2)
	v_mfma_f32_16x16x32_bf16 v[166:169], v[202:205], v[232:235], v[166:169]
	s_and_b64 vcc, exec, s[6:7]
	v_mfma_f32_16x16x32_bf16 v[158:161], v[198:201], v[232:235], v[158:161]
	s_waitcnt lgkmcnt(1)
	v_mfma_f32_16x16x32_bf16 v[150:153], v[206:209], v[232:235], v[150:153]
	s_waitcnt lgkmcnt(0)
	v_mfma_f32_16x16x32_bf16 v[154:157], v[210:213], v[232:235], v[154:157]
	s_cbranch_vccnz .LBB0_1550
	ds_read_b128 v[232:235], v3 offset:2048
	s_waitcnt lgkmcnt(0)
	v_mfma_f32_16x16x32_bf16 v[134:137], v[198:201], v[232:235], v[134:137]
	v_mfma_f32_16x16x32_bf16 v[146:149], v[202:205], v[232:235], v[146:149]
	v_mfma_f32_16x16x32_bf16 v[102:105], v[206:209], v[232:235], v[102:105]
	v_mfma_f32_16x16x32_bf16 v[106:109], v[210:213], v[232:235], v[106:109]
	v_cndmask_b32_e64 v5, 0, 1, s[54:55]
	v_cmp_ne_u32_e64 s[8:9], 1, v5
	s_andn2_b64 vcc, exec, s[54:55]
	s_cbranch_vccz .LBB0_1551
